# P5 conversion fp8 stores: nt sc1 (write-through, non-temporal) instead of nt
# baseline (speedup 1.0000x reference)
; #define GAS __attribute__((address_space(1)))
; #define LAS __attribute__((address_space(3)))
; __device__ __forceinline__ void tr_flush(LAS unsigned* img, int K, int N, unsigned char* WT, size_t row_off, int fl, int lane) {
;     ...
;     for (int p = 0; p < CPR; ++p) { const int n = lane / CPR + RPP * p;
;         const v4u o = *(const LAS v4u*)(img + n * (16 * NHB) + 4 * (c ^ ((n >> 2) & 7)));
;         *(GAS v4u*)(WT + (row_off + n0 + n) * (size_t)K + k0 + 16 * c) = o; }
.LBB0_551:
	s_add_i32 s9, s8, -3
	s_add_i32 s11, s8, -2
	s_add_i32 s35, s8, -1
	v_bitop3_b32 v8, s9, v213, 4 bitop3:0x6c
	v_bitop3_b32 v9, s11, v213, 5 bitop3:0x6c
	v_bitop3_b32 v10, s35, v213, 6 bitop3:0x6c
	v_lshl_add_u64 v[26:27], v[2:3], 0, v[198:199]
	v_bitop3_b32 v7, s8, v213, 7 bitop3:0x6c
	v_lshl_add_u32 v8, v8, 4, v6
	v_lshl_add_u32 v12, v9, 4, v6
	v_lshl_add_u32 v16, v10, 4, v6
	v_add_co_u32_e32 v28, vcc, s14, v26
	v_lshl_add_u32 v7, v7, 4, v6
	ds_read_b128 v[8:11], v8
	ds_read_b128 v[12:15], v12 offset:1024
	ds_read_b128 v[16:19], v16 offset:2048
	ds_read_b128 v[20:23], v7 offset:3072
	v_addc_co_u32_e32 v29, vcc, 0, v27, vcc
	v_add_co_u32_e32 v30, vcc, s15, v26
	s_add_i32 s8, s8, 4
	s_nop 0
	v_addc_co_u32_e32 v31, vcc, 0, v27, vcc
	v_lshl_add_u64 v[24:25], v[4:5], 0, v[198:199]
	v_lshl_add_u64 v[2:3], v[2:3], 0, s[4:5]
	v_lshl_add_u64 v[4:5], v[4:5], 0, s[4:5]
	s_cmp_lg_u32 s8, 19
	v_add_u32_e32 v6, 0x1000, v6
	v_add_co_u32_e32 v26, vcc, 0x68c0e000, v26
	s_nop 1
	v_addc_co_u32_e32 v27, vcc, 0, v27, vcc
	s_waitcnt lgkmcnt(3)
	global_store_dwordx4 v[24:25], v[8:11], off nt sc1
	s_waitcnt lgkmcnt(2)
	global_store_dwordx4 v[28:29], v[12:15], off nt sc1
	s_waitcnt lgkmcnt(1)
	global_store_dwordx4 v[30:31], v[16:19], off nt sc1
	s_waitcnt lgkmcnt(0)
	global_store_dwordx4 v[26:27], v[20:23], off nt sc1
	s_cbranch_scc1 .LBB0_551
	s_waitcnt lgkmcnt(0)
	s_mov_b64 s[8:9], 0

; #define GAS __attribute__((address_space(1)))
; #define LAS __attribute__((address_space(3)))
; __device__ __forceinline__ void tr_flush(LAS unsigned* img, int K, int N, unsigned char* WT, size_t row_off, int fl, int lane) {
;     ...
;     for (int p = 0; p < CPR; ++p) { const int n = lane / CPR + RPP * p;
;         const v4u o = *(const LAS v4u*)(img + n * (16 * NHB) + 4 * (c ^ ((n >> 2) & 7)));
;         *(GAS v4u*)(WT + (row_off + n0 + n) * (size_t)K + k0 + 16 * c) = o; }
.LBB0_555:
	s_add_i32 s7, s6, -3
	s_add_i32 s10, s6, -2
	s_add_i32 s11, s6, -1
	v_bitop3_b32 v8, s7, v213, 4 bitop3:0x6c
	v_bitop3_b32 v9, s10, v213, 5 bitop3:0x6c
	v_bitop3_b32 v10, s11, v213, 6 bitop3:0x6c
	v_lshl_add_u64 v[26:27], v[2:3], 0, s[8:9]
	v_bitop3_b32 v7, s6, v213, 7 bitop3:0x6c
	v_lshl_add_u32 v8, v8, 4, v6
	v_lshl_add_u32 v12, v9, 4, v6
	v_lshl_add_u32 v16, v10, 4, v6
	v_add_co_u32_e32 v28, vcc, s16, v26
	v_lshl_add_u32 v7, v7, 4, v6
	ds_read_b128 v[8:11], v8
	ds_read_b128 v[12:15], v12 offset:1024
	ds_read_b128 v[16:19], v16 offset:2048
	ds_read_b128 v[20:23], v7 offset:3072
	v_addc_co_u32_e32 v29, vcc, 0, v27, vcc
	v_add_co_u32_e32 v30, vcc, s17, v26
	s_add_i32 s6, s6, 4
	s_nop 0
	v_addc_co_u32_e32 v31, vcc, 0, v27, vcc
	v_lshl_add_u64 v[24:25], v[4:5], 0, s[8:9]
	v_lshl_add_u64 v[2:3], v[2:3], 0, s[4:5]
	v_lshl_add_u64 v[4:5], v[4:5], 0, s[4:5]
	s_cmp_lg_u32 s6, 19
	v_add_u32_e32 v6, 0x1000, v6
	v_add_co_u32_e32 v26, vcc, 0x58c0e000, v26
	s_nop 1
	v_addc_co_u32_e32 v27, vcc, 0, v27, vcc
	s_waitcnt lgkmcnt(3)
	global_store_dwordx4 v[24:25], v[8:11], off nt sc1
	s_waitcnt lgkmcnt(2)
	global_store_dwordx4 v[28:29], v[12:15], off nt sc1
	s_waitcnt lgkmcnt(1)
	global_store_dwordx4 v[30:31], v[16:19], off nt sc1
	s_waitcnt lgkmcnt(0)
	global_store_dwordx4 v[26:27], v[20:23], off nt sc1
	s_cbranch_scc1 .LBB0_555
	s_waitcnt lgkmcnt(0)

; #define GAS __attribute__((address_space(1)))
; #define LAS __attribute__((address_space(3)))
; __device__ __forceinline__ void tr_flush(LAS unsigned* img, int K, int N, unsigned char* WT, size_t row_off, int fl, int lane) {
;     ...
;     for (int p = 0; p < CPR; ++p) { const int n = lane / CPR + RPP * p;
;         const v4u o = *(const LAS v4u*)(img + n * (16 * NHB) + 4 * (c ^ ((n >> 2) & 7)));
;         *(GAS v4u*)(WT + (row_off + n0 + n) * (size_t)K + k0 + 16 * c) = o; }
.LBB0_565:
	s_add_i32 s9, s8, -3
	s_add_i32 s11, s8, -2
	s_add_i32 s36, s8, -1
	v_bitop3_b32 v72, s9, v213, 4 bitop3:0x6c
	v_bitop3_b32 v73, s11, v213, 5 bitop3:0x6c
	v_bitop3_b32 v74, s36, v213, 6 bitop3:0x6c
	v_lshl_add_u64 v[90:91], v[66:67], 0, v[198:199]
	v_bitop3_b32 v71, s8, v213, 7 bitop3:0x6c
	v_lshl_add_u32 v72, v72, 4, v70
	v_lshl_add_u32 v76, v73, 4, v70
	v_lshl_add_u32 v80, v74, 4, v70
	v_add_co_u32_e32 v92, vcc, s14, v90
	v_lshl_add_u32 v71, v71, 4, v70
	ds_read_b128 v[72:75], v72
	ds_read_b128 v[76:79], v76 offset:1024
	ds_read_b128 v[80:83], v80 offset:2048
	ds_read_b128 v[84:87], v71 offset:3072
	v_addc_co_u32_e32 v93, vcc, 0, v91, vcc
	v_add_co_u32_e32 v94, vcc, s15, v90
	s_add_i32 s8, s8, 4
	s_nop 0
	v_addc_co_u32_e32 v95, vcc, 0, v91, vcc
	v_lshl_add_u64 v[88:89], v[68:69], 0, v[198:199]
	v_lshl_add_u64 v[66:67], v[66:67], 0, s[4:5]
	v_lshl_add_u64 v[68:69], v[68:69], 0, s[4:5]
	s_cmp_lg_u32 s8, 19
	v_add_u32_e32 v70, 0x1000, v70
	v_add_co_u32_e32 v90, vcc, 0x68c0e000, v90
	s_nop 1
	v_addc_co_u32_e32 v91, vcc, 0, v91, vcc
	s_waitcnt lgkmcnt(3)
	global_store_dwordx4 v[88:89], v[72:75], off nt sc1
	s_waitcnt lgkmcnt(2)
	global_store_dwordx4 v[92:93], v[76:79], off nt sc1
	s_waitcnt lgkmcnt(1)
	global_store_dwordx4 v[94:95], v[80:83], off nt sc1
	s_waitcnt lgkmcnt(0)
	global_store_dwordx4 v[90:91], v[84:87], off nt sc1
	s_cbranch_scc1 .LBB0_565
	s_waitcnt lgkmcnt(0)
	s_mov_b64 s[8:9], 0

; #define GAS __attribute__((address_space(1)))
; #define LAS __attribute__((address_space(3)))
; __device__ __forceinline__ void tr_flush(LAS unsigned* img, int K, int N, unsigned char* WT, size_t row_off, int fl, int lane) {
;     ...
;     for (int p = 0; p < CPR; ++p) { const int n = lane / CPR + RPP * p;
;         const v4u o = *(const LAS v4u*)(img + n * (16 * NHB) + 4 * (c ^ ((n >> 2) & 7)));
;         *(GAS v4u*)(WT + (row_off + n0 + n) * (size_t)K + k0 + 16 * c) = o; }
.LBB0_569:
	s_add_i32 s7, s6, -3
	s_add_i32 s10, s6, -2
	s_add_i32 s11, s6, -1
	v_bitop3_b32 v72, s7, v213, 4 bitop3:0x6c
	v_bitop3_b32 v73, s10, v213, 5 bitop3:0x6c
	v_bitop3_b32 v74, s11, v213, 6 bitop3:0x6c
	v_lshl_add_u64 v[90:91], v[66:67], 0, s[8:9]
	v_bitop3_b32 v71, s6, v213, 7 bitop3:0x6c
	v_lshl_add_u32 v72, v72, 4, v70
	v_lshl_add_u32 v76, v73, 4, v70
	v_lshl_add_u32 v80, v74, 4, v70
	v_add_co_u32_e32 v92, vcc, s16, v90
	v_lshl_add_u32 v71, v71, 4, v70
	ds_read_b128 v[72:75], v72
	ds_read_b128 v[76:79], v76 offset:1024
	ds_read_b128 v[80:83], v80 offset:2048
	ds_read_b128 v[84:87], v71 offset:3072
	v_addc_co_u32_e32 v93, vcc, 0, v91, vcc
	v_add_co_u32_e32 v94, vcc, s17, v90
	s_add_i32 s6, s6, 4
	s_nop 0
	v_addc_co_u32_e32 v95, vcc, 0, v91, vcc
	v_lshl_add_u64 v[88:89], v[68:69], 0, s[8:9]
	v_lshl_add_u64 v[66:67], v[66:67], 0, s[4:5]
	v_lshl_add_u64 v[68:69], v[68:69], 0, s[4:5]
	s_cmp_lg_u32 s6, 19
	v_add_u32_e32 v70, 0x1000, v70
	v_add_co_u32_e32 v90, vcc, 0x58c0e000, v90
	s_nop 1
	v_addc_co_u32_e32 v91, vcc, 0, v91, vcc
	s_waitcnt lgkmcnt(3)
	global_store_dwordx4 v[88:89], v[72:75], off nt sc1
	s_waitcnt lgkmcnt(2)
	global_store_dwordx4 v[92:93], v[76:79], off nt sc1
	s_waitcnt lgkmcnt(1)
	global_store_dwordx4 v[94:95], v[80:83], off nt sc1
	s_waitcnt lgkmcnt(0)
	global_store_dwordx4 v[90:91], v[84:87], off nt sc1
	s_cbranch_scc1 .LBB0_569
	s_waitcnt lgkmcnt(0)

; #define GAS __attribute__((address_space(1)))
; #define LAS __attribute__((address_space(3)))
; __device__ __forceinline__ void tr_flush(LAS unsigned* img, int K, int N, unsigned char* WT, size_t row_off, int fl, int lane) {
;     ...
;     for (int p = 0; p < CPR; ++p) { const int n = lane / CPR + RPP * p;
;         const v4u o = *(const LAS v4u*)(img + n * (16 * NHB) + 4 * (c ^ ((n >> 2) & 7)));
;         *(GAS v4u*)(WT + (row_off + n0 + n) * (size_t)K + k0 + 16 * c) = o; }
.LBB0_579:
	s_add_i32 s9, s8, -3
	s_add_i32 s11, s8, -2
	s_add_i32 s31, s8, -1
	v_bitop3_b32 v136, s9, v213, 4 bitop3:0x6c
	v_bitop3_b32 v137, s11, v213, 5 bitop3:0x6c
	v_bitop3_b32 v138, s31, v213, 6 bitop3:0x6c
	v_lshl_add_u64 v[154:155], v[130:131], 0, v[198:199]
	v_bitop3_b32 v135, s8, v213, 7 bitop3:0x6c
	v_lshl_add_u32 v136, v136, 4, v134
	v_lshl_add_u32 v140, v137, 4, v134
	v_lshl_add_u32 v144, v138, 4, v134
	v_add_co_u32_e32 v156, vcc, s14, v154
	v_lshl_add_u32 v135, v135, 4, v134
	ds_read_b128 v[136:139], v136
	ds_read_b128 v[140:143], v140 offset:1024
	ds_read_b128 v[144:147], v144 offset:2048
	ds_read_b128 v[148:151], v135 offset:3072
	v_addc_co_u32_e32 v157, vcc, 0, v155, vcc
	v_add_co_u32_e32 v158, vcc, s15, v154
	s_add_i32 s8, s8, 4
	s_nop 0
	v_addc_co_u32_e32 v159, vcc, 0, v155, vcc
	v_lshl_add_u64 v[152:153], v[132:133], 0, v[198:199]
	v_lshl_add_u64 v[130:131], v[130:131], 0, s[4:5]
	v_lshl_add_u64 v[132:133], v[132:133], 0, s[4:5]
	s_cmp_lg_u32 s8, 19
	v_add_u32_e32 v134, 0x1000, v134
	v_add_co_u32_e32 v154, vcc, 0x68c0e000, v154
	s_nop 1
	v_addc_co_u32_e32 v155, vcc, 0, v155, vcc
	s_waitcnt lgkmcnt(3)
	global_store_dwordx4 v[152:153], v[136:139], off nt sc1
	s_waitcnt lgkmcnt(2)
	global_store_dwordx4 v[156:157], v[140:143], off nt sc1
	s_waitcnt lgkmcnt(1)
	global_store_dwordx4 v[158:159], v[144:147], off nt sc1
	s_waitcnt lgkmcnt(0)
	global_store_dwordx4 v[154:155], v[148:151], off nt sc1
	s_cbranch_scc1 .LBB0_579
	s_waitcnt lgkmcnt(0)
	s_mov_b64 s[8:9], 0

; #define GAS __attribute__((address_space(1)))
; #define LAS __attribute__((address_space(3)))
; __device__ __forceinline__ void tr_flush(LAS unsigned* img, int K, int N, unsigned char* WT, size_t row_off, int fl, int lane) {
;     ...
;     for (int p = 0; p < CPR; ++p) { const int n = lane / CPR + RPP * p;
;         const v4u o = *(const LAS v4u*)(img + n * (16 * NHB) + 4 * (c ^ ((n >> 2) & 7)));
;         *(GAS v4u*)(WT + (row_off + n0 + n) * (size_t)K + k0 + 16 * c) = o; }
.LBB0_583:
	s_add_i32 s7, s6, -3
	s_add_i32 s10, s6, -2
	s_add_i32 s11, s6, -1
	v_bitop3_b32 v136, s7, v213, 4 bitop3:0x6c
	v_bitop3_b32 v137, s10, v213, 5 bitop3:0x6c
	v_bitop3_b32 v138, s11, v213, 6 bitop3:0x6c
	v_lshl_add_u64 v[154:155], v[130:131], 0, s[8:9]
	v_bitop3_b32 v135, s6, v213, 7 bitop3:0x6c
	v_lshl_add_u32 v136, v136, 4, v134
	v_lshl_add_u32 v140, v137, 4, v134
	v_lshl_add_u32 v144, v138, 4, v134
	v_add_co_u32_e32 v156, vcc, s16, v154
	v_lshl_add_u32 v135, v135, 4, v134
	ds_read_b128 v[136:139], v136
	ds_read_b128 v[140:143], v140 offset:1024
	ds_read_b128 v[144:147], v144 offset:2048
	ds_read_b128 v[148:151], v135 offset:3072
	v_addc_co_u32_e32 v157, vcc, 0, v155, vcc
	v_add_co_u32_e32 v158, vcc, s17, v154
	s_add_i32 s6, s6, 4
	s_nop 0
	v_addc_co_u32_e32 v159, vcc, 0, v155, vcc
	v_lshl_add_u64 v[152:153], v[132:133], 0, s[8:9]
	v_lshl_add_u64 v[130:131], v[130:131], 0, s[4:5]
	v_lshl_add_u64 v[132:133], v[132:133], 0, s[4:5]
	s_cmp_lg_u32 s6, 19
	v_add_u32_e32 v134, 0x1000, v134
	v_add_co_u32_e32 v154, vcc, 0x58c0e000, v154
	s_nop 1
	v_addc_co_u32_e32 v155, vcc, 0, v155, vcc
	s_waitcnt lgkmcnt(3)
	global_store_dwordx4 v[152:153], v[136:139], off nt sc1
	s_waitcnt lgkmcnt(2)
	global_store_dwordx4 v[156:157], v[140:143], off nt sc1
	s_waitcnt lgkmcnt(1)
	global_store_dwordx4 v[158:159], v[144:147], off nt sc1
	s_waitcnt lgkmcnt(0)
	global_store_dwordx4 v[154:155], v[148:151], off nt sc1
	s_cbranch_scc1 .LBB0_583
	s_waitcnt lgkmcnt(0)
	s_branch .LBB0_542
